# m5 + removed 40 redundant register copies per chunk from the scan helper waves
# speedup vs baseline: 1.0059x; 1.0059x over previous
; __device__ __forceinline__ void scan_head(const Params& p, LAS unsigned char* lds, int bh, const int wave) {
;     ...
;         } else {
;             if (chunk + 1 < NCH) SCAN_ISSUE(chunk + 1);
;             if (chunk > 0) SCAN_POST(chunk - 1);
;             if (chunk + 1 < NCH) SCAN_STAGE(chunk + 1);
;         }
.LBB0_789:
	s_waitcnt vmcnt(0)
	s_mov_b32 s51, s2

; __device__ __forceinline__ void scan_head(const Params& p, LAS unsigned char* lds, int bh, const int wave) {
;     ...
;         } else {
;             if (chunk + 1 < NCH) SCAN_ISSUE(chunk + 1);
;             if (chunk > 0) SCAN_POST(chunk - 1);
;             if (chunk + 1 < NCH) SCAN_STAGE(chunk + 1);
;         }
.LBB0_791:
	s_mov_b64 s[14:15], -1
	s_and_b64 vcc, exec, s[42:43]
	s_cbranch_vccz .LBB0_806
	s_add_i32 s52, s51, 1
	s_cmp_lg_u32 s51, 63
	s_cselect_b64 s[14:15], -1, 0
	s_cmp_eq_u32 s51, 63
	s_cbranch_scc1 .LBB0_794
	v_lshl_or_b32 v10, s52, 5, v125
	v_mov_b32_e32 v11, v48
	v_lshl_add_u64 v[10:11], s[40:41], 0, v[10:11]
	v_mov_b64_e32 v[12:13], s[58:59]
	v_mad_u64_u32 v[12:13], s[60:61], v10, s35, v[12:13]
	v_mov_b32_e32 v8, v124
	v_mov_b32_e32 v14, v13
	v_mad_u64_u32 v[14:15], s[60:61], v11, s35, v[14:15]
	v_ashrrev_i32_e32 v9, 31, v8
	v_mov_b32_e32 v13, v14
	v_lshlrev_b64 v[14:15], 1, v[8:9]
	v_lshl_add_u64 v[12:13], v[12:13], 0, v[14:15]
	s_movk_i32 s2, 0x1000
	v_add_co_u32_e32 v50, vcc, s2, v12
	s_movk_i32 s2, 0xc000
	s_nop 0
	v_addc_co_u32_e32 v51, vcc, 0, v13, vcc
	v_add_co_u32_e32 v80, vcc, s2, v12
	s_movk_i32 s2, 0xd000
	s_nop 0
	v_addc_co_u32_e32 v81, vcc, -1, v13, vcc
	global_load_dwordx4 v[72:75], v[12:13], off
	global_load_dwordx4 v[68:71], v[12:13], off offset:2048
	v_add_co_u32_e32 v12, vcc, s2, v12
	global_load_dwordx4 v[76:79], v[50:51], off
	s_nop 0
	global_load_dwordx4 v[80:83], v[80:81], off offset:-1024
	v_addc_co_u32_e32 v13, vcc, -1, v13, vcc
	global_load_dwordx4 v[88:91], v[12:13], off offset:-3072
	global_load_dwordx4 v[84:87], v[12:13], off offset:-1024
	v_lshlrev_b64 v[12:13], 11, v[10:11]
	v_lshlrev_b64 v[10:11], 12, v[10:11]
	v_lshl_add_u64 v[50:51], s[66:67], 0, v[12:13]
	v_lshl_add_u64 v[12:13], s[68:69], 0, v[12:13]
	v_lshl_add_u64 v[10:11], s[64:65], 0, v[10:11]
	v_lshl_add_u64 v[50:51], v[50:51], 0, v[14:15]
	v_lshl_add_u64 v[12:13], v[12:13], 0, v[14:15]
	v_lshl_add_u64 v[8:9], v[8:9], 2, v[10:11]
	global_load_dwordx4 v[92:95], v[50:51], off nt
	global_load_dwordx4 v[96:99], v[12:13], off nt
	s_nop 0
	global_load_dwordx4 v[12:15], v[8:9], off offset:16 nt
	s_nop 0
	global_load_dwordx4 v[8:11], v[8:9], off nt
